# speedup vs baseline: 1.0084x; 1.0084x over previous
.LBB2_129:
	s_or_b64 exec, exec, s[4:5]
	s_and_b64 vcc, exec, s[2:3]
	s_waitcnt lgkmcnt(0)
	s_barrier
	s_cbranch_vccnz .LBB2_131
	v_lshlrev_b32_e32 v6, 5, v0
	v_lshrrev_b32_e32 v2, 2, v0
	v_lshlrev_b32_e32 v3, 2, v0
	v_and_b32_e32 v4, 0x60, v6
	s_movk_i32 s2, 0x310
	v_mad_u32_u24 v7, v2, s2, v4
	v_and_b32_e32 v2, 16, v3
	v_lshlrev_b32_e32 v13, 1, v0
	v_and_or_b32 v10, v13, 32, v2
	ds_read_b128 v[2:5], v7 offset:640
	v_and_b32_e32 v8, 3, v0
	s_movk_i32 s2, 0x3c08
	v_bitop3_b32 v11, v6, s2, v0 bitop3:0xc8
	v_lshlrev_b32_e32 v12, 1, v8
	s_waitcnt lgkmcnt(0)
	v_bfe_u32 v13, v2, 16, 1
	s_movk_i32 s2, 0x7fff
	v_lshlrev_b32_e32 v10, 4, v10
	v_add3_u32 v2, v2, v13, s2
	v_or3_b32 v10, v11, v12, v10
	ds_write_b16_d16_hi v10, v2 offset:50176
	v_bfe_u32 v2, v3, 16, 1
	ds_read_b128 v[6:9], v7 offset:656
	v_add3_u32 v2, v3, v2, s2
	ds_write_b16_d16_hi v10, v2 offset:50192
	v_bfe_u32 v2, v4, 16, 1
	v_add3_u32 v2, v4, v2, s2
	ds_write_b16_d16_hi v10, v2 offset:50208
	v_bfe_u32 v2, v5, 16, 1
	v_add3_u32 v2, v5, v2, s2
	ds_write_b16_d16_hi v10, v2 offset:50224
	s_waitcnt lgkmcnt(3)
	v_bfe_u32 v2, v6, 16, 1
	v_add3_u32 v2, v6, v2, s2
	ds_write_b16_d16_hi v10, v2 offset:50240
	v_bfe_u32 v2, v7, 16, 1
	v_add3_u32 v2, v7, v2, s2
	ds_write_b16_d16_hi v10, v2 offset:50256
	v_bfe_u32 v2, v8, 16, 1
	v_add3_u32 v2, v8, v2, s2
	ds_write_b16_d16_hi v10, v2 offset:50272
	v_bfe_u32 v2, v9, 16, 1
	v_add3_u32 v2, v9, v2, s2
	ds_write_b16_d16_hi v10, v2 offset:50288

_Z6k_attnPKDv8_DF16_PKfPKhS3_S3_S3_PfS6_S3_S3_PS_S7_:
	v_readfirstlane_b32 s3, v0
	s_cmpk_lt_u32 s2, 0x1a4
	s_mov_b64 s[4:5], -1
	s_cbranch_scc0 .LBB3_37
	s_cmpk_lt_u32 s2, 0x104
	s_cbranch_scc0 .LBB3_27
	s_cmpk_lt_u32 s2, 0x100
	s_cbranch_scc0 .LBB3_20
	s_lshr_b32 s5, s3, 6
	s_lshl_b32 s3, s2, 1
	s_lshr_b32 s10, s2, 1
	s_bfe_u32 s4, s2, 0x20001
	s_and_b32 s3, s3, 2
	s_bfe_u32 s11, s2, 0x10003
	s_load_dwordx2 s[6:7], s[0:1], 0x0
	s_load_dwordx2 s[8:9], s[0:1], 0x10
	s_load_dwordx2 s[20:21], s[0:1], 0x38
	s_or_b32 s3, s3, s11
	s_lshl_b32 s11, s4, 7
	s_and_b32 s10, s10, 0x78
	s_or_b32 s10, s11, s10
	s_add_i32 s5, s10, s5
	s_lshl_b32 s10, s3, 17
	s_lshl_b32 s11, s4, 19
	s_or_b32 s10, s10, s11
	s_waitcnt lgkmcnt(0)
	s_add_u32 s8, s8, s10
	v_mov_b32_e32 v18, 0
	s_addc_u32 s9, s9, 0
	s_add_u32 s28, s8, 0x10000
	s_addc_u32 s29, s9, 0
	s_add_u32 s30, s8, 0x12000
	s_addc_u32 s31, s9, 0
	s_add_u32 s32, s8, 0x14000
	s_addc_u32 s33, s9, 0
	s_add_u32 s34, s8, 0x16000
	s_addc_u32 s35, s9, 0
	s_add_u32 s36, s8, 0x18000
	s_addc_u32 s37, s9, 0
	s_add_u32 s38, s8, 0x1a000
	s_addc_u32 s39, s9, 0
	s_add_u32 s40, s8, 0x1c000
	s_addc_u32 s41, s9, 0
	s_add_u32 s42, s8, 0x1e000
	s_addc_u32 s43, s9, 0
	v_lshlrev_b32_e32 v88, 4, v0
	v_mov_b32_e32 v89, v18
	v_lshl_add_u64 v[2:3], s[8:9], 0, v[88:89]
	global_load_dwordx4 v[40:43], v88, s[8:9]
	s_movk_i32 s8, 0x2000
	v_add_co_u32_e32 v4, vcc, s8, v2
	s_movk_i32 s8, 0x4000
	s_nop 0
	v_addc_co_u32_e32 v5, vcc, 0, v3, vcc
	v_add_co_u32_e32 v6, vcc, s8, v2
	s_movk_i32 s8, 0x6000
	s_nop 0
	v_addc_co_u32_e32 v7, vcc, 0, v3, vcc
	global_load_dwordx4 v[44:47], v[4:5], off
	global_load_dwordx4 v[48:51], v[6:7], off
	v_add_co_u32_e32 v4, vcc, s8, v2
	s_mov_b32 s8, 0x8000
	s_nop 0
	v_addc_co_u32_e32 v5, vcc, 0, v3, vcc
	v_add_co_u32_e32 v6, vcc, s8, v2
	s_mov_b32 s8, 0xa000
	s_nop 0
	v_addc_co_u32_e32 v7, vcc, 0, v3, vcc
	global_load_dwordx4 v[52:55], v[4:5], off
	global_load_dwordx4 v[56:59], v[6:7], off
	v_add_co_u32_e32 v4, vcc, s8, v2
	s_mov_b32 s8, 0xc000
	s_nop 0
	v_addc_co_u32_e32 v5, vcc, 0, v3, vcc
	v_add_co_u32_e32 v6, vcc, s8, v2
	s_mov_b32 s8, 0xe000
	s_nop 0
	v_addc_co_u32_e32 v7, vcc, 0, v3, vcc
	global_load_dwordx4 v[60:63], v[4:5], off
	global_load_dwordx4 v[64:67], v[6:7], off
	v_add_co_u32_e32 v4, vcc, s8, v2
	v_and_b32_e32 v1, 63, v0
	s_nop 0
	v_addc_co_u32_e32 v5, vcc, 0, v3, vcc
	s_mul_i32 s8, s5, 0xc0
	global_load_dwordx4 v[68:71], v[4:5], off
	v_or_b32_e32 v4, s8, v1
	v_mov_b32_e32 v5, v18
	s_add_i32 s9, s8, 64
	v_lshl_add_u64 v[4:5], v[4:5], 4, s[6:7]
	v_or_b32_e32 v6, s9, v1
	v_mov_b32_e32 v7, v18
	s_addk_i32 s8, 0x80
	v_lshl_add_u64 v[6:7], v[6:7], 4, s[6:7]
	global_load_dwordx4 v[72:75], v[4:5], off
	global_load_dwordx4 v[76:79], v[6:7], off
	v_or_b32_e32 v4, s8, v1
	v_mov_b32_e32 v5, v18
	v_lshl_add_u64 v[4:5], v[4:5], 4, s[6:7]
	global_load_dwordx4 v[80:83], v[4:5], off
	s_lshl_b32 s24, s5, 5
	v_cmp_lt_u32_e32 vcc, 31, v1
	s_and_saveexec_b64 s[22:23], vcc
	s_cbranch_execz .LBB3_5
	s_load_dwordx2 s[6:7], s[0:1], 0x8
	s_load_dwordx2 s[26:27], s[0:1], 0x18
	v_and_or_b32 v4, v0, 31, s24
	v_mov_b32_e32 v5, 0
	s_lshl_b32 s25, s4, 6
	s_waitcnt lgkmcnt(0)
	v_lshl_add_u64 v[4:5], v[4:5], 2, s[6:7]
	global_load_dword v4, v[4:5], off
	s_load_dwordx16 s[4:19], s[26:27], s25 offset:0x0
	s_waitcnt lgkmcnt(0)
	v_max_f32_e64 v5, s4, s4
	v_mov_b32_e32 v6, s6
	v_max_f32_e32 v5, 0, v5
	v_mov_b32_e32 v7, s8
	v_min3_f32 v5, -v5, -s5, -v6
	v_mov_b32_e32 v8, s10
	v_min3_f32 v5, v5, -s7, -v7
	v_mov_b32_e32 v9, s12
	v_min3_f32 v5, v5, -s9, -v8
	v_mov_b32_e32 v10, s14
	v_min3_f32 v5, v5, -s11, -v9
	v_mov_b32_e32 v11, s16
	v_min3_f32 v5, v5, -s13, -v10
	v_mov_b32_e32 v12, s18
	v_min3_f32 v5, v5, -s15, -v11
	v_max_f32_e64 v13, -s19, -s19
	v_min3_f32 v5, v5, -s17, -v12
	v_min_f32_e32 v5, v5, v13
	s_mov_b32 s4, 0xffff
	s_waitcnt vmcnt(0)
	v_fma_mixlo_f16 v4, v4, v5, 0
	v_bfi_b32 v80, s4, v4, v80
.LBB3_5:
	s_or_b64 exec, exec, s[22:23]
	s_mov_b64 s[4:5], 0x10000
	s_mov_b64 s[4:5], 0x12000
	s_mov_b64 s[4:5], 0x14000
	s_mov_b64 s[4:5], 0x16000
	s_mov_b64 s[4:5], 0x18000
	s_mov_b64 s[4:5], 0x1a000
	s_mov_b64 s[4:5], 0x1c000
	s_mov_b64 s[4:5], 0x1e000
	v_lshlrev_b32_e32 v89, 4, v1
	v_mov_b32_e32 v90, 0
	v_mov_b32_e32 v91, 0
	v_mov_b32_e32 v92, 0
	v_mov_b32_e32 v93, 0
	v_mov_b32_e32 v94, 0
	v_mov_b32_e32 v95, 0
	v_mov_b32_e32 v96, 0
	v_mov_b32_e32 v97, 0
	v_mov_b32_e32 v98, 0
	v_mov_b32_e32 v99, 0
	v_mov_b32_e32 v100, 0
	v_mov_b32_e32 v101, 0
	v_mov_b32_e32 v102, 0
	v_mov_b32_e32 v103, 0
	v_mov_b32_e32 v104, 0
	v_mov_b32_e32 v105, 0
	v_and_b32_e32 v126, 31, v1
	v_min_u32_e32 v126, 15, v126
	v_lshrrev_b32_e32 v127, 5, v1
	v_lshl_or_b32 v126, v127, 4, v126
	v_lshlrev_b32_e32 v126, 4, v126
	s_mov_b64 s[6:7], 0
	s_mov_b64 s[4:5], -1
	v_mov_b32_e32 v19, v18
	v_mov_b32_e32 v20, v18
	v_mov_b32_e32 v21, v18
	v_mov_b32_e32 v84, v18
	v_mov_b32_e32 v85, v18
	v_mov_b32_e32 v86, v18
	v_mov_b32_e32 v87, v18
	s_waitcnt vmcnt(10)
	ds_write_b128 v88, v[40:43]
	s_waitcnt vmcnt(9)
	ds_write_b128 v88, v[44:47] offset:8192
	s_waitcnt vmcnt(8)
	ds_write_b128 v88, v[48:51] offset:16384
	s_waitcnt vmcnt(7)
	ds_write_b128 v88, v[52:55] offset:24576
	s_waitcnt lgkmcnt(0)
	s_barrier
	s_branch .LBB3_7
.LBB3_6:
	ds_read_b128 v[2:5], v89 offset:32768
	ds_read_b128 v[22:25], v89 offset:33792
	s_xor_b64 s[8:9], s[4:5], -1
	s_mov_b64 s[6:7], -1
	s_mov_b64 s[4:5], 0
	s_waitcnt lgkmcnt(1)
	v_mfma_f32_32x32x16_f16 v[2:17], v[2:5], v[72:75], 0
	s_and_b64 vcc, exec, s[8:9]
	s_waitcnt lgkmcnt(0)
	v_mfma_f32_32x32x16_f16 v[2:17], v[22:25], v[76:79], v[2:17]
	ds_read_b128 v[22:25], v89 offset:36864
	ds_read_b128 v[106:109], v89 offset:37888
	ds_read_b128 v[110:113], v89 offset:34816
	ds_read_b128 v[114:117], v89 offset:38912
	ds_read_b128 v[118:121], v126 offset:35840
	ds_read_b128 v[18:21], v126 offset:36352
	s_waitcnt lgkmcnt(5)
	v_mfma_f32_32x32x16_f16 v[24:39], v[22:25], v[72:75], 0
	s_waitcnt lgkmcnt(4)
	v_mfma_f32_32x32x16_f16 v[24:39], v[106:109], v[76:79], v[24:39]
	s_waitcnt lgkmcnt(3)
	v_mfma_f32_32x32x16_f16 v[2:17], v[110:113], v[80:83], v[2:17]
	s_waitcnt lgkmcnt(2)
	v_mfma_f32_32x32x16_f16 v[24:39], v[114:117], v[80:83], v[24:39]
	s_nop 9
	v_exp_f32_e32 v2, v2
	v_exp_f32_e32 v22, v3
	v_exp_f32_e32 v3, v4
	v_exp_f32_e32 v23, v5
	v_exp_f32_e32 v4, v6
	v_exp_f32_e32 v6, v7
	v_exp_f32_e32 v5, v8
	v_exp_f32_e32 v7, v9
	v_exp_f32_e32 v10, v10
	v_exp_f32_e32 v11, v11
	v_exp_f32_e32 v12, v12
	v_exp_f32_e32 v13, v13
	v_exp_f32_e32 v8, v14
	v_exp_f32_e32 v14, v15
	v_exp_f32_e32 v9, v16
	v_exp_f32_e32 v15, v17
	v_cvt_pk_bf16_f32 v5, v5, v7
	v_cvt_pk_bf16_f32 v4, v4, v6
	v_cvt_pk_bf16_f32 v3, v3, v23
	v_cvt_pk_bf16_f32 v2, v2, v22
	v_cvt_pk_bf16_f32 v9, v9, v15
	v_cvt_pk_bf16_f32 v8, v8, v14
	v_cvt_pk_bf16_f32 v7, v12, v13
	v_cvt_pk_bf16_f32 v6, v10, v11
	s_nop 1
	v_exp_f32_e32 v114, v24
	v_exp_f32_e32 v22, v26
	v_exp_f32_e32 v23, v28
	v_exp_f32_e32 v24, v30
	s_waitcnt lgkmcnt(1)
	s_waitcnt lgkmcnt(0)
	v_mfma_f32_32x32x16_bf16 v[90:105], v[18:21], v[6:9], v[90:105]
	ds_read_b128 v[10:13], v126 offset:39936
	ds_read_b128 v[14:17], v89 offset:40960
	ds_read_b128 v[106:109], v89 offset:41984
	ds_read_b128 v[110:113], v89 offset:43008
	v_exp_f32_e32 v18, v31
	v_exp_f32_e32 v19, v29
	v_exp_f32_e32 v20, v27
	v_mfma_f32_32x32x16_bf16 v[90:105], v[118:121], v[2:5], v[90:105]
	ds_read_b128 v[6:9], v126 offset:40448
	s_nop 2
	v_exp_f32_e32 v84, v25
	v_cvt_pk_bf16_f32 v87, v24, v18
	v_cvt_pk_bf16_f32 v86, v23, v19
	v_cvt_pk_bf16_f32 v85, v22, v20
	s_waitcnt lgkmcnt(3)
	v_mfma_f32_32x32x16_f16 v[16:31], v[14:17], v[72:75], 0
	v_exp_f32_e32 v14, v32
	v_exp_f32_e32 v15, v34
	v_exp_f32_e32 v32, v36
	v_exp_f32_e32 v34, v37
	v_exp_f32_e32 v36, v38
	v_exp_f32_e32 v37, v39
	v_exp_f32_e32 v38, v35
	s_waitcnt lgkmcnt(2)
	v_mfma_f32_32x32x16_f16 v[16:31], v[106:109], v[76:79], v[16:31]
	v_exp_f32_e32 v39, v33
	v_cvt_pk_bf16_f32 v84, v114, v84
	v_cvt_pk_bf16_f32 v35, v36, v37
	v_cvt_pk_bf16_f32 v34, v32, v34
	v_cvt_pk_bf16_f32 v33, v15, v38
	v_cvt_pk_bf16_f32 v32, v14, v39
	s_nop 1
	ds_read_b128 v[36:39], v126 offset:44032
	s_nop 0
	v_mfma_f32_32x32x16_bf16 v[90:105], v[10:13], v[84:87], v[90:105]
	s_nop 2
	ds_read_b128 v[2:5], v89 offset:45056
	s_waitcnt lgkmcnt(3)
	v_mfma_f32_32x32x16_f16 v[16:31], v[110:113], v[80:83], v[16:31]
	s_waitcnt lgkmcnt(2)
	v_mfma_f32_32x32x16_bf16 v[90:105], v[6:9], v[32:35], v[90:105]
	ds_read_b128 v[106:109], v126 offset:44544
	s_nop 10
	v_exp_f32_e32 v114, v16
	v_exp_f32_e32 v118, v17
	v_exp_f32_e32 v18, v18
	s_waitcnt lgkmcnt(1)
	v_mfma_f32_32x32x16_f16 v[2:17], v[2:5], v[72:75], 0
	v_exp_f32_e32 v20, v20
	v_exp_f32_e32 v21, v21
	v_exp_f32_e32 v19, v19
	ds_read_b128 v[32:35], v89 offset:46080
	ds_read_b128 v[110:113], v89 offset:47104
	v_cvt_pk_bf16_f32 v114, v114, v118
	v_cvt_pk_bf16_f32 v116, v20, v21
	v_cvt_pk_bf16_f32 v115, v18, v19
	ds_read_b128 v[118:121], v126 offset:48128
	ds_read_b128 v[18:21], v89 offset:49152
	v_exp_f32_e32 v22, v22
	v_exp_f32_e32 v23, v23
	s_waitcnt lgkmcnt(3)
	v_mfma_f32_32x32x16_f16 v[2:17], v[32:35], v[76:79], v[2:17]
	v_exp_f32_e32 v29, v29
	v_exp_f32_e32 v27, v27
	v_cvt_pk_bf16_f32 v117, v22, v23
	v_exp_f32_e32 v22, v24
	v_exp_f32_e32 v23, v26
	v_exp_f32_e32 v24, v28
	v_exp_f32_e32 v26, v30
	v_exp_f32_e32 v28, v31
	v_exp_f32_e32 v25, v25
	ds_read_b128 v[122:125], v89 offset:50176
	s_waitcnt lgkmcnt(3)
	v_mfma_f32_32x32x16_f16 v[2:17], v[110:113], v[80:83], v[2:17]
	v_cvt_pk_bf16_f32 v113, v26, v28
	v_cvt_pk_bf16_f32 v112, v24, v29
	v_cvt_pk_bf16_f32 v111, v23, v27
	v_cvt_pk_bf16_f32 v110, v22, v25
	s_nop 1
	s_waitcnt lgkmcnt(1)
	v_mfma_f32_32x32x16_f16 v[18:33], v[18:21], v[72:75], 0
	v_exp_f32_e32 v2, v2
	v_exp_f32_e32 v4, v4
	v_exp_f32_e32 v5, v5
	v_mfma_f32_32x32x16_bf16 v[90:105], v[36:39], v[114:117], v[90:105]
	v_exp_f32_e32 v3, v3
	v_exp_f32_e32 v6, v6
	v_exp_f32_e32 v7, v7
	s_waitcnt lgkmcnt(5)
	v_mfma_f32_32x32x16_bf16 v[90:105], v[106:109], v[110:113], v[90:105]
	ds_read_b128 v[34:37], v126 offset:48640
	ds_read_b128 v[84:87], v126 offset:52736
	ds_read_b128 v[110:113], v126 offset:52224
	v_exp_f32_e32 v8, v8
	v_exp_f32_e32 v9, v9
	ds_read_b128 v[106:109], v89 offset:51200
	s_waitcnt lgkmcnt(4)
	v_mfma_f32_32x32x16_f16 v[18:33], v[122:125], v[76:79], v[18:33]
	v_exp_f32_e32 v13, v13
	v_exp_f32_e32 v11, v11
	ds_read_b128 v[122:125], v89 offset:54272
	s_waitcnt lgkmcnt(1)
	v_mfma_f32_32x32x16_f16 v[18:33], v[106:109], v[80:83], v[18:33]
	v_cvt_pk_bf16_f32 v107, v4, v5
	v_cvt_pk_bf16_f32 v106, v2, v3
	ds_read_b128 v[2:5], v89 offset:53248
	v_cvt_pk_bf16_f32 v109, v8, v9
	v_cvt_pk_bf16_f32 v108, v6, v7
	v_exp_f32_e32 v6, v10
	v_exp_f32_e32 v7, v12
	v_exp_f32_e32 v8, v14
	v_exp_f32_e32 v9, v16
	v_exp_f32_e32 v10, v17
	v_exp_f32_e32 v12, v15
	v_cvt_pk_bf16_f32 v115, v7, v13
	v_cvt_pk_bf16_f32 v114, v6, v11
	v_cvt_pk_bf16_f32 v117, v9, v10
	v_cvt_pk_bf16_f32 v116, v8, v12
	s_waitcnt lgkmcnt(0)
	v_mfma_f32_32x32x16_f16 v[2:17], v[2:5], v[72:75], 0
	v_mfma_f32_32x32x16_f16 v[2:17], v[122:125], v[76:79], v[2:17]
	v_exp_f32_e32 v18, v18
	v_exp_f32_e32 v20, v20
	v_exp_f32_e32 v21, v21
	v_exp_f32_e32 v19, v19
	v_exp_f32_e32 v22, v22
	v_exp_f32_e32 v24, v24
	v_exp_f32_e32 v25, v25
	v_mfma_f32_32x32x16_bf16 v[90:105], v[118:121], v[106:109], v[90:105]
	v_exp_f32_e32 v23, v23
	v_exp_f32_e32 v29, v29
	v_exp_f32_e32 v27, v27
	s_waitcnt lgkmcnt(5)
	v_mfma_f32_32x32x16_bf16 v[90:105], v[34:37], v[114:117], v[90:105]
	ds_read_b128 v[106:109], v89 offset:55296
	ds_read_b128 v[114:117], v126 offset:56320
	ds_read_b128 v[34:37], v126 offset:56832
	ds_read_b128 v[122:125], v89 offset:58368
	s_waitcnt lgkmcnt(3)
	v_mfma_f32_32x32x16_f16 v[2:17], v[106:109], v[80:83], v[2:17]
	v_cvt_pk_bf16_f32 v107, v20, v21
	v_cvt_pk_bf16_f32 v106, v18, v19
	ds_read_b128 v[18:21], v89 offset:57344
	v_cvt_pk_bf16_f32 v109, v24, v25
	v_cvt_pk_bf16_f32 v108, v22, v23
	v_exp_f32_e32 v22, v26
	v_exp_f32_e32 v23, v28
	v_exp_f32_e32 v24, v30
	v_exp_f32_e32 v25, v32
	v_exp_f32_e32 v26, v33
	v_exp_f32_e32 v28, v31
	v_cvt_pk_bf16_f32 v119, v23, v29
	v_cvt_pk_bf16_f32 v118, v22, v27
	v_cvt_pk_bf16_f32 v121, v25, v26
	v_cvt_pk_bf16_f32 v120, v24, v28
	s_waitcnt lgkmcnt(0)
	v_mfma_f32_32x32x16_f16 v[18:33], v[18:21], v[72:75], 0
	v_mfma_f32_32x32x16_f16 v[18:33], v[122:125], v[76:79], v[18:33]
	v_exp_f32_e32 v2, v2
	v_exp_f32_e32 v4, v4
	v_exp_f32_e32 v5, v5
	v_exp_f32_e32 v3, v3
	v_exp_f32_e32 v6, v6
	v_exp_f32_e32 v8, v8
	v_exp_f32_e32 v9, v9
	v_mfma_f32_32x32x16_bf16 v[90:105], v[110:113], v[106:109], v[90:105]
	v_exp_f32_e32 v7, v7
	v_exp_f32_e32 v13, v13
	v_exp_f32_e32 v11, v11
	s_waitcnt lgkmcnt(9)
	v_mfma_f32_32x32x16_bf16 v[90:105], v[84:87], v[118:121], v[90:105]
	ds_read_b128 v[106:109], v89 offset:59392
	ds_read_b128 v[110:113], v126 offset:60416
	ds_read_b128 v[84:87], v126 offset:60928
	ds_read_b128 v[122:125], v89 offset:62464
	s_waitcnt lgkmcnt(3)
	v_mfma_f32_32x32x16_f16 v[18:33], v[106:109], v[80:83], v[18:33]
	v_cvt_pk_bf16_f32 v107, v4, v5
	v_cvt_pk_bf16_f32 v106, v2, v3
	ds_read_b128 v[2:5], v89 offset:61440
	v_cvt_pk_bf16_f32 v109, v8, v9
	v_cvt_pk_bf16_f32 v108, v6, v7
	v_exp_f32_e32 v6, v10
	v_exp_f32_e32 v7, v12
	v_exp_f32_e32 v8, v14
	v_exp_f32_e32 v9, v16
	v_exp_f32_e32 v10, v17
	v_exp_f32_e32 v12, v15
	v_cvt_pk_bf16_f32 v119, v7, v13
	v_cvt_pk_bf16_f32 v118, v6, v11
	v_cvt_pk_bf16_f32 v121, v9, v10
	v_cvt_pk_bf16_f32 v120, v8, v12
	s_waitcnt lgkmcnt(0)
	v_mfma_f32_32x32x16_f16 v[2:17], v[2:5], v[72:75], 0
	v_mfma_f32_32x32x16_f16 v[2:17], v[122:125], v[76:79], v[2:17]
	v_exp_f32_e32 v38, v20
	v_exp_f32_e32 v20, v22
	v_exp_f32_e32 v22, v24
	v_exp_f32_e32 v24, v25
	v_exp_f32_e32 v25, v21
	v_exp_f32_e32 v23, v23
	v_exp_f32_e32 v39, v19
	v_mfma_f32_32x32x16_bf16 v[90:105], v[114:117], v[106:109], v[90:105]
	v_cvt_pk_bf16_f32 v21, v22, v24
	v_cvt_pk_bf16_f32 v19, v38, v25
	v_exp_f32_e32 v22, v26
	s_waitcnt lgkmcnt(7)
	v_mfma_f32_32x32x16_bf16 v[90:105], v[34:37], v[118:121], v[90:105]
	ds_read_b128 v[106:109], v89 offset:63488
	ds_read_b128 v[114:117], v126 offset:64512
	ds_read_b128 v[34:37], v126 offset:65024
	v_exp_f32_e32 v25, v32
	v_exp_f32_e32 v26, v33
	s_waitcnt lgkmcnt(2)
	v_mfma_f32_32x32x16_f16 v[2:17], v[106:109], v[80:83], v[2:17]
	v_exp_f32_e32 v18, v18
	v_cvt_pk_bf16_f32 v20, v20, v23
	v_exp_f32_e32 v23, v28
	v_exp_f32_e32 v24, v30
	v_exp_f32_e32 v28, v31
	v_exp_f32_e32 v29, v29
	v_exp_f32_e32 v27, v27
	v_cvt_pk_bf16_f32 v25, v25, v26
	s_nop 3
	v_exp_f32_e32 v26, v4
	v_exp_f32_e32 v4, v6
	v_exp_f32_e32 v6, v8
	v_exp_f32_e32 v8, v9
	v_exp_f32_e32 v7, v7
	v_exp_f32_e32 v9, v5
	v_cvt_pk_bf16_f32 v18, v18, v39
	v_cvt_pk_bf16_f32 v24, v24, v28
	v_cvt_pk_bf16_f32 v23, v23, v29
	v_cvt_pk_bf16_f32 v22, v22, v27
	v_exp_f32_e32 v2, v2
	v_exp_f32_e32 v27, v3
	v_cvt_pk_bf16_f32 v5, v6, v8
	v_cvt_pk_bf16_f32 v4, v4, v7
	v_cvt_pk_bf16_f32 v3, v26, v9
	v_exp_f32_e32 v6, v10
	v_exp_f32_e32 v7, v12
	v_exp_f32_e32 v8, v14
	v_exp_f32_e32 v9, v16
	v_exp_f32_e32 v10, v17
	v_exp_f32_e32 v12, v15
	v_exp_f32_e32 v13, v13
	v_exp_f32_e32 v11, v11
	v_cvt_pk_bf16_f32 v2, v2, v27
	s_nop 0
	v_mfma_f32_32x32x16_bf16 v[90:105], v[110:113], v[18:21], v[90:105]
	v_cvt_pk_bf16_f32 v9, v9, v10
	v_cvt_pk_bf16_f32 v8, v8, v12
	v_cvt_pk_bf16_f32 v7, v7, v13
	s_waitcnt lgkmcnt(5)
	v_mfma_f32_32x32x16_bf16 v[90:105], v[84:87], v[22:25], v[90:105]
	v_cvt_pk_bf16_f32 v6, v6, v11
	s_nop 1
	s_waitcnt lgkmcnt(0)
	s_nop 0
	v_mfma_f32_32x32x16_bf16 v[90:105], v[114:117], v[2:5], v[90:105]
	s_barrier
	s_waitcnt lgkmcnt(0)
	v_mfma_f32_32x32x16_bf16 v[90:105], v[34:37], v[6:9], v[90:105]
	s_cbranch_vccnz .LBB3_13
.LBB3_7:
	s_and_b64 vcc, exec, s[4:5]
	s_waitcnt vmcnt(3)
	ds_write_b128 v88, v[56:59] offset:32768
	s_waitcnt vmcnt(2)
	ds_write_b128 v88, v[60:63] offset:40960
	s_waitcnt vmcnt(1)
	ds_write_b128 v88, v[64:67] offset:49152
	s_waitcnt vmcnt(0)
	ds_write_b128 v88, v[68:71] offset:57344
	s_cbranch_vccz .LBB3_9
	global_load_dwordx4 v[40:43], v88, s[28:29]
	global_load_dwordx4 v[44:47], v88, s[30:31]
	global_load_dwordx4 v[48:51], v88, s[32:33]
	global_load_dwordx4 v[52:55], v88, s[34:35]
.LBB3_9:
	ds_read_b128 v[2:5], v89
	ds_read_b128 v[22:25], v89 offset:1024
	s_xor_b64 s[6:7], s[6:7], -1
	s_andn2_b64 vcc, exec, s[6:7]
	s_waitcnt lgkmcnt(1)
	v_mfma_f32_32x32x16_f16 v[2:17], v[2:5], v[72:75], 0
	s_waitcnt lgkmcnt(0)
	v_mfma_f32_32x32x16_f16 v[2:17], v[22:25], v[76:79], v[2:17]
	ds_read_b128 v[22:25], v89 offset:4096
	ds_read_b128 v[106:109], v89 offset:5120
	ds_read_b128 v[110:113], v89 offset:2048
	ds_read_b128 v[114:117], v89 offset:6144
	ds_read_b128 v[118:121], v126 offset:3072
	ds_read_b128 v[18:21], v126 offset:3584
	s_waitcnt lgkmcnt(5)
	v_mfma_f32_32x32x16_f16 v[24:39], v[22:25], v[72:75], 0
	s_waitcnt lgkmcnt(4)
	v_mfma_f32_32x32x16_f16 v[24:39], v[106:109], v[76:79], v[24:39]
	s_waitcnt lgkmcnt(3)
	v_mfma_f32_32x32x16_f16 v[2:17], v[110:113], v[80:83], v[2:17]
	s_waitcnt lgkmcnt(2)
	v_mfma_f32_32x32x16_f16 v[24:39], v[114:117], v[80:83], v[24:39]
	s_nop 9
	v_exp_f32_e32 v2, v2
	v_exp_f32_e32 v22, v3
	v_exp_f32_e32 v3, v4
	v_exp_f32_e32 v23, v5
	v_exp_f32_e32 v4, v6
	v_exp_f32_e32 v6, v7
	v_exp_f32_e32 v5, v8
	v_exp_f32_e32 v7, v9
	v_exp_f32_e32 v10, v10
	v_exp_f32_e32 v11, v11
	v_exp_f32_e32 v12, v12
	v_exp_f32_e32 v13, v13
	v_exp_f32_e32 v8, v14
	v_exp_f32_e32 v14, v15
	v_exp_f32_e32 v9, v16
	v_exp_f32_e32 v15, v17
	v_cvt_pk_bf16_f32 v5, v5, v7
	v_cvt_pk_bf16_f32 v4, v4, v6
	v_cvt_pk_bf16_f32 v3, v3, v23
	v_cvt_pk_bf16_f32 v2, v2, v22
	v_cvt_pk_bf16_f32 v9, v9, v15
	v_cvt_pk_bf16_f32 v8, v8, v14
	v_cvt_pk_bf16_f32 v7, v12, v13
	v_cvt_pk_bf16_f32 v6, v10, v11
	s_nop 1
	v_exp_f32_e32 v114, v24
	v_exp_f32_e32 v22, v26
	v_exp_f32_e32 v23, v28
	v_exp_f32_e32 v24, v30
	s_waitcnt lgkmcnt(1)
	s_waitcnt lgkmcnt(0)
	v_mfma_f32_32x32x16_bf16 v[90:105], v[18:21], v[6:9], v[90:105]
	ds_read_b128 v[10:13], v126 offset:7168
	ds_read_b128 v[14:17], v89 offset:8192
	ds_read_b128 v[106:109], v89 offset:9216
	ds_read_b128 v[110:113], v89 offset:10240
	v_exp_f32_e32 v18, v31
	v_exp_f32_e32 v19, v29
	v_exp_f32_e32 v20, v27
	v_mfma_f32_32x32x16_bf16 v[90:105], v[118:121], v[2:5], v[90:105]
	ds_read_b128 v[6:9], v126 offset:7680
	s_nop 2
	v_exp_f32_e32 v84, v25
	v_cvt_pk_bf16_f32 v87, v24, v18
	v_cvt_pk_bf16_f32 v86, v23, v19
	v_cvt_pk_bf16_f32 v85, v22, v20
	s_waitcnt lgkmcnt(3)
	v_mfma_f32_32x32x16_f16 v[16:31], v[14:17], v[72:75], 0
	v_exp_f32_e32 v14, v32
	v_exp_f32_e32 v15, v34
	v_exp_f32_e32 v32, v36
	v_exp_f32_e32 v34, v37
	v_exp_f32_e32 v36, v38
	v_exp_f32_e32 v37, v39
	v_exp_f32_e32 v38, v35
	s_waitcnt lgkmcnt(2)
	v_mfma_f32_32x32x16_f16 v[16:31], v[106:109], v[76:79], v[16:31]
	v_exp_f32_e32 v39, v33
	v_cvt_pk_bf16_f32 v84, v114, v84
	v_cvt_pk_bf16_f32 v35, v36, v37
	v_cvt_pk_bf16_f32 v34, v32, v34
	v_cvt_pk_bf16_f32 v33, v15, v38
	v_cvt_pk_bf16_f32 v32, v14, v39
	s_nop 1
	ds_read_b128 v[36:39], v126 offset:11264
	s_nop 0
	v_mfma_f32_32x32x16_bf16 v[90:105], v[10:13], v[84:87], v[90:105]
	s_nop 2
	ds_read_b128 v[2:5], v89 offset:12288
	s_waitcnt lgkmcnt(3)
	v_mfma_f32_32x32x16_f16 v[16:31], v[110:113], v[80:83], v[16:31]
	s_waitcnt lgkmcnt(2)
	v_mfma_f32_32x32x16_bf16 v[90:105], v[6:9], v[32:35], v[90:105]
	ds_read_b128 v[106:109], v126 offset:11776
	s_nop 10
	v_exp_f32_e32 v114, v16
	v_exp_f32_e32 v118, v17
	v_exp_f32_e32 v18, v18
	s_waitcnt lgkmcnt(1)
	v_mfma_f32_32x32x16_f16 v[2:17], v[2:5], v[72:75], 0
	v_exp_f32_e32 v20, v20
	v_exp_f32_e32 v21, v21
	v_exp_f32_e32 v19, v19
	ds_read_b128 v[32:35], v89 offset:13312
	ds_read_b128 v[110:113], v89 offset:14336
	v_cvt_pk_bf16_f32 v114, v114, v118
	v_cvt_pk_bf16_f32 v116, v20, v21
	v_cvt_pk_bf16_f32 v115, v18, v19
	ds_read_b128 v[118:121], v126 offset:15360
	ds_read_b128 v[18:21], v89 offset:16384
	v_exp_f32_e32 v22, v22
	v_exp_f32_e32 v23, v23
	s_waitcnt lgkmcnt(3)
	v_mfma_f32_32x32x16_f16 v[2:17], v[32:35], v[76:79], v[2:17]
	v_exp_f32_e32 v29, v29
	v_exp_f32_e32 v27, v27
	v_cvt_pk_bf16_f32 v117, v22, v23
	v_exp_f32_e32 v22, v24
	v_exp_f32_e32 v23, v26
	v_exp_f32_e32 v24, v28
	v_exp_f32_e32 v26, v30
	v_exp_f32_e32 v28, v31
	v_exp_f32_e32 v25, v25
	ds_read_b128 v[122:125], v89 offset:17408
	s_waitcnt lgkmcnt(3)
	v_mfma_f32_32x32x16_f16 v[2:17], v[110:113], v[80:83], v[2:17]
	v_cvt_pk_bf16_f32 v113, v26, v28
	v_cvt_pk_bf16_f32 v112, v24, v29
	v_cvt_pk_bf16_f32 v111, v23, v27
	v_cvt_pk_bf16_f32 v110, v22, v25
	s_nop 1
	s_waitcnt lgkmcnt(1)
	v_mfma_f32_32x32x16_f16 v[18:33], v[18:21], v[72:75], 0
	v_exp_f32_e32 v2, v2
	v_exp_f32_e32 v4, v4
	v_exp_f32_e32 v5, v5
	v_mfma_f32_32x32x16_bf16 v[90:105], v[36:39], v[114:117], v[90:105]
	v_exp_f32_e32 v3, v3
	v_exp_f32_e32 v6, v6
	v_exp_f32_e32 v7, v7
	s_waitcnt lgkmcnt(5)
	v_mfma_f32_32x32x16_bf16 v[90:105], v[106:109], v[110:113], v[90:105]
	ds_read_b128 v[34:37], v126 offset:15872
	ds_read_b128 v[84:87], v126 offset:19968
	ds_read_b128 v[110:113], v126 offset:19456
	v_exp_f32_e32 v8, v8
	v_exp_f32_e32 v9, v9
	ds_read_b128 v[106:109], v89 offset:18432
	s_waitcnt lgkmcnt(4)
	v_mfma_f32_32x32x16_f16 v[18:33], v[122:125], v[76:79], v[18:33]
	v_exp_f32_e32 v13, v13
	v_exp_f32_e32 v11, v11
	ds_read_b128 v[122:125], v89 offset:21504
	s_waitcnt lgkmcnt(1)
	v_mfma_f32_32x32x16_f16 v[18:33], v[106:109], v[80:83], v[18:33]
	v_cvt_pk_bf16_f32 v107, v4, v5
	v_cvt_pk_bf16_f32 v106, v2, v3
	ds_read_b128 v[2:5], v89 offset:20480
	v_cvt_pk_bf16_f32 v109, v8, v9
	v_cvt_pk_bf16_f32 v108, v6, v7
	v_exp_f32_e32 v6, v10
	v_exp_f32_e32 v7, v12
	v_exp_f32_e32 v8, v14
	v_exp_f32_e32 v9, v16
	v_exp_f32_e32 v10, v17
	v_exp_f32_e32 v12, v15
	v_cvt_pk_bf16_f32 v115, v7, v13
	v_cvt_pk_bf16_f32 v114, v6, v11
	v_cvt_pk_bf16_f32 v117, v9, v10
	v_cvt_pk_bf16_f32 v116, v8, v12
	s_waitcnt lgkmcnt(0)
	v_mfma_f32_32x32x16_f16 v[2:17], v[2:5], v[72:75], 0
	v_mfma_f32_32x32x16_f16 v[2:17], v[122:125], v[76:79], v[2:17]
	v_exp_f32_e32 v18, v18
	v_exp_f32_e32 v20, v20
	v_exp_f32_e32 v21, v21
	v_exp_f32_e32 v19, v19
	v_exp_f32_e32 v22, v22
	v_exp_f32_e32 v24, v24
	v_exp_f32_e32 v25, v25
	v_mfma_f32_32x32x16_bf16 v[90:105], v[118:121], v[106:109], v[90:105]
	v_exp_f32_e32 v23, v23
	v_exp_f32_e32 v29, v29
	v_exp_f32_e32 v27, v27
	s_waitcnt lgkmcnt(5)
	v_mfma_f32_32x32x16_bf16 v[90:105], v[34:37], v[114:117], v[90:105]
	ds_read_b128 v[106:109], v89 offset:22528
	ds_read_b128 v[114:117], v126 offset:23552
	ds_read_b128 v[34:37], v126 offset:24064
	ds_read_b128 v[122:125], v89 offset:25600
	s_waitcnt lgkmcnt(3)
	v_mfma_f32_32x32x16_f16 v[2:17], v[106:109], v[80:83], v[2:17]
	v_cvt_pk_bf16_f32 v107, v20, v21
	v_cvt_pk_bf16_f32 v106, v18, v19
	ds_read_b128 v[18:21], v89 offset:24576
	v_cvt_pk_bf16_f32 v109, v24, v25
	v_cvt_pk_bf16_f32 v108, v22, v23
	v_exp_f32_e32 v22, v26
	v_exp_f32_e32 v23, v28
	v_exp_f32_e32 v24, v30
	v_exp_f32_e32 v25, v32
	v_exp_f32_e32 v26, v33
	v_exp_f32_e32 v28, v31
	v_cvt_pk_bf16_f32 v119, v23, v29
	v_cvt_pk_bf16_f32 v118, v22, v27
	v_cvt_pk_bf16_f32 v121, v25, v26
	v_cvt_pk_bf16_f32 v120, v24, v28
	s_waitcnt lgkmcnt(0)
	v_mfma_f32_32x32x16_f16 v[18:33], v[18:21], v[72:75], 0
	v_mfma_f32_32x32x16_f16 v[18:33], v[122:125], v[76:79], v[18:33]
	v_exp_f32_e32 v2, v2
	v_exp_f32_e32 v4, v4
	v_exp_f32_e32 v5, v5
	v_exp_f32_e32 v3, v3
	v_exp_f32_e32 v6, v6
	v_exp_f32_e32 v8, v8
	v_exp_f32_e32 v9, v9
	v_mfma_f32_32x32x16_bf16 v[90:105], v[110:113], v[106:109], v[90:105]
	v_exp_f32_e32 v7, v7
	v_exp_f32_e32 v13, v13
	v_exp_f32_e32 v11, v11
	s_waitcnt lgkmcnt(9)
	v_mfma_f32_32x32x16_bf16 v[90:105], v[84:87], v[118:121], v[90:105]
	ds_read_b128 v[106:109], v89 offset:26624
	ds_read_b128 v[110:113], v126 offset:27648
	ds_read_b128 v[84:87], v126 offset:28160
	ds_read_b128 v[122:125], v89 offset:29696
	s_waitcnt lgkmcnt(3)
	v_mfma_f32_32x32x16_f16 v[18:33], v[106:109], v[80:83], v[18:33]
	v_cvt_pk_bf16_f32 v107, v4, v5
	v_cvt_pk_bf16_f32 v106, v2, v3
	ds_read_b128 v[2:5], v89 offset:28672
	v_cvt_pk_bf16_f32 v109, v8, v9
	v_cvt_pk_bf16_f32 v108, v6, v7
	v_exp_f32_e32 v6, v10
	v_exp_f32_e32 v7, v12
	v_exp_f32_e32 v8, v14
	v_exp_f32_e32 v9, v16
	v_exp_f32_e32 v10, v17
	v_exp_f32_e32 v12, v15
	v_cvt_pk_bf16_f32 v119, v7, v13
	v_cvt_pk_bf16_f32 v118, v6, v11
	v_cvt_pk_bf16_f32 v121, v9, v10
	v_cvt_pk_bf16_f32 v120, v8, v12
	s_waitcnt lgkmcnt(0)
	v_mfma_f32_32x32x16_f16 v[2:17], v[2:5], v[72:75], 0
	v_mfma_f32_32x32x16_f16 v[2:17], v[122:125], v[76:79], v[2:17]
	v_exp_f32_e32 v38, v20
	v_exp_f32_e32 v20, v22
	v_exp_f32_e32 v22, v24
	v_exp_f32_e32 v24, v25
	v_exp_f32_e32 v25, v21
	v_exp_f32_e32 v23, v23
	v_exp_f32_e32 v39, v19
	v_mfma_f32_32x32x16_bf16 v[90:105], v[114:117], v[106:109], v[90:105]
	v_cvt_pk_bf16_f32 v21, v22, v24
	v_cvt_pk_bf16_f32 v19, v38, v25
	v_exp_f32_e32 v22, v26
	s_waitcnt lgkmcnt(7)
	v_mfma_f32_32x32x16_bf16 v[90:105], v[34:37], v[118:121], v[90:105]
	ds_read_b128 v[106:109], v89 offset:30720
	ds_read_b128 v[114:117], v126 offset:31744
	ds_read_b128 v[34:37], v126 offset:32256
	v_exp_f32_e32 v25, v32
	v_exp_f32_e32 v26, v33
	s_waitcnt lgkmcnt(2)
	v_mfma_f32_32x32x16_f16 v[2:17], v[106:109], v[80:83], v[2:17]
	v_exp_f32_e32 v18, v18
	v_cvt_pk_bf16_f32 v20, v20, v23
	v_exp_f32_e32 v23, v28
	v_exp_f32_e32 v24, v30
	v_exp_f32_e32 v28, v31
	v_exp_f32_e32 v29, v29
	v_exp_f32_e32 v27, v27
	v_cvt_pk_bf16_f32 v25, v25, v26
	s_nop 3
	v_exp_f32_e32 v26, v4
	v_exp_f32_e32 v4, v6
	v_exp_f32_e32 v6, v8
	v_exp_f32_e32 v8, v9
	v_exp_f32_e32 v7, v7
	v_exp_f32_e32 v9, v5
	v_cvt_pk_bf16_f32 v18, v18, v39
	v_cvt_pk_bf16_f32 v24, v24, v28
	v_cvt_pk_bf16_f32 v23, v23, v29
	v_cvt_pk_bf16_f32 v22, v22, v27
	v_exp_f32_e32 v2, v2
	v_exp_f32_e32 v27, v3
	v_cvt_pk_bf16_f32 v5, v6, v8
	v_cvt_pk_bf16_f32 v4, v4, v7
	v_cvt_pk_bf16_f32 v3, v26, v9
	v_exp_f32_e32 v6, v10
	v_exp_f32_e32 v7, v12
	v_exp_f32_e32 v8, v14
	v_exp_f32_e32 v9, v16
	v_exp_f32_e32 v10, v17
	v_exp_f32_e32 v12, v15
	v_exp_f32_e32 v13, v13
	v_exp_f32_e32 v11, v11
	v_cvt_pk_bf16_f32 v2, v2, v27
	s_nop 0
	v_mfma_f32_32x32x16_bf16 v[90:105], v[110:113], v[18:21], v[90:105]
	v_cvt_pk_bf16_f32 v9, v9, v10
	v_cvt_pk_bf16_f32 v8, v8, v12
	v_cvt_pk_bf16_f32 v7, v7, v13
	s_waitcnt lgkmcnt(5)
	v_mfma_f32_32x32x16_bf16 v[90:105], v[84:87], v[22:25], v[90:105]
	v_cvt_pk_bf16_f32 v6, v6, v11
	s_nop 1
	s_waitcnt lgkmcnt(0)
	s_nop 0
	v_mfma_f32_32x32x16_bf16 v[90:105], v[114:117], v[2:5], v[90:105]
	s_barrier
	s_waitcnt lgkmcnt(0)
	v_mfma_f32_32x32x16_bf16 v[90:105], v[34:37], v[6:9], v[90:105]
	s_cbranch_vccnz .LBB3_11
	s_waitcnt vmcnt(0)
	ds_write_b128 v88, v[40:43]
	ds_write_b128 v88, v[44:47] offset:8192
	ds_write_b128 v88, v[48:51] offset:16384
	ds_write_b128 v88, v[52:55] offset:24576
.LBB3_11:
	s_andn2_b64 vcc, exec, s[4:5]
	s_cbranch_vccnz .LBB3_6
	global_load_dwordx4 v[56:59], v88, s[36:37]
	global_load_dwordx4 v[60:63], v88, s[38:39]
	global_load_dwordx4 v[64:67], v88, s[40:41]
	global_load_dwordx4 v[68:71], v88, s[42:43]
	s_branch .LBB3_6
.LBB3_13:
	s_lshl_b32 s3, s3, 14
	s_add_i32 s24, s24, s3
	v_and_or_b32 v2, v0, 31, s24
	v_mad_u64_u32 v[2:3], s[4:5], v2, 48, s[20:21]
	v_lshrrev_b32_e32 v4, 5, v1
	v_lshlrev_b32_e32 v4, 4, v4
	v_mov_b32_e32 v5, 0
	v_lshl_add_u64 v[2:3], v[2:3], 0, v[4:5]
	s_nop 15
	global_store_dwordx4 v[2:3], v[90:93], off
	v_cmp_gt_u32_e32 vcc, 32, v1
	s_and_saveexec_b64 s[4:5], vcc
	s_cbranch_execz .LBB3_19
	global_store_dword v[2:3], v94, off offset:32

	.amdhsa_kernel _Z6k_attnPKDv8_DF16_PKfPKhS3_S3_S3_PfS6_S3_S3_PS_S7_
		.amdhsa_group_segment_fixed_size 65536
		.amdhsa_private_segment_fixed_size 0
		.amdhsa_kernarg_size 96
		.amdhsa_user_sgpr_count 2
		.amdhsa_user_sgpr_dispatch_ptr 0
		.amdhsa_user_sgpr_queue_ptr 0
		.amdhsa_user_sgpr_kernarg_segment_ptr 1
		.amdhsa_user_sgpr_dispatch_id 0
		.amdhsa_user_sgpr_kernarg_preload_length 0
		.amdhsa_user_sgpr_kernarg_preload_offset 0
		.amdhsa_user_sgpr_private_segment_size 0
		.amdhsa_uses_dynamic_stack 0
		.amdhsa_enable_private_segment 0
		.amdhsa_system_sgpr_workgroup_id_x 1
		.amdhsa_system_sgpr_workgroup_id_y 0
		.amdhsa_system_sgpr_workgroup_id_z 0
		.amdhsa_system_sgpr_workgroup_info 0
		.amdhsa_system_vgpr_workitem_id 0
		.amdhsa_next_free_vgpr 128
		.amdhsa_next_free_sgpr 96
		.amdhsa_accum_offset 128
		.amdhsa_reserve_vcc 1
		.amdhsa_float_round_mode_32 0
		.amdhsa_float_round_mode_16_64 0
		.amdhsa_float_denorm_mode_32 3
		.amdhsa_float_denorm_mode_16_64 3
		.amdhsa_dx10_clamp 1
		.amdhsa_ieee_mode 1
		.amdhsa_fp16_overflow 0
		.amdhsa_tg_split 0
		.amdhsa_exception_fp_ieee_invalid_op 0
		.amdhsa_exception_fp_denorm_src 0
		.amdhsa_exception_fp_ieee_div_zero 0
		.amdhsa_exception_fp_ieee_overflow 0
		.amdhsa_exception_fp_ieee_underflow 0
		.amdhsa_exception_fp_ieee_inexact 0
		.amdhsa_exception_int_div_zero 0
	.end_amdhsa_kernel

amdhsa.kernels:
  - .agpr_count:     0
    .args:
      - .actual_access:  read_only
        .address_space:  global
        .offset:         0
        .size:           8
        .value_kind:     global_buffer
      - .actual_access:  read_only
        .address_space:  global
        .offset:         8
        .size:           8
        .value_kind:     global_buffer
      - .actual_access:  read_only
        .address_space:  global
        .offset:         16
        .size:           8
        .value_kind:     global_buffer
      - .actual_access:  read_only
        .address_space:  global
        .offset:         24
        .size:           8
        .value_kind:     global_buffer
      - .actual_access:  read_only
        .address_space:  global
        .offset:         32
        .size:           8
        .value_kind:     global_buffer
      - .actual_access:  read_only
        .address_space:  global
        .offset:         40
        .size:           8
        .value_kind:     global_buffer
      - .actual_access:  read_only
        .address_space:  global
        .offset:         48
        .size:           8
        .value_kind:     global_buffer
      - .actual_access:  write_only
        .address_space:  global
        .offset:         56
        .size:           8
        .value_kind:     global_buffer
    .group_segment_fixed_size: 98304
    .kernarg_segment_align: 8
    .kernarg_segment_size: 64
    .language:       OpenCL C
    .language_version:
      - 2
      - 0
    .max_flat_workgroup_size: 512
    .name:           _Z11k_conv_mfmaPKDF16_PKDv8_DF16_PKfS5_S5_S5_S5_PDF16_
    .private_segment_fixed_size: 0
    .sgpr_count:     36
    .sgpr_spill_count: 0
    .symbol:         _Z11k_conv_mfmaPKDF16_PKDv8_DF16_PKfS5_S5_S5_S5_PDF16_.kd
    .uniform_work_group_size: 1
    .uses_dynamic_stack: false
    .vgpr_count:     164
    .vgpr_spill_count: 0
    .wavefront_size: 64
  - .agpr_count:     0
    .args:
      - .actual_access:  read_only
        .address_space:  global
        .offset:         0
        .size:           8
        .value_kind:     global_buffer
      - .actual_access:  read_only
        .address_space:  global
        .offset:         8
        .size:           8
        .value_kind:     global_buffer
      - .actual_access:  read_only
        .address_space:  global
        .offset:         16
        .size:           8
        .value_kind:     global_buffer
      - .actual_access:  write_only
        .address_space:  global
        .offset:         24
        .size:           8
        .value_kind:     global_buffer
    .group_segment_fixed_size: 25600
    .kernarg_segment_align: 8
    .kernarg_segment_size: 32
    .language:       OpenCL C
    .language_version:
      - 2
      - 0
    .max_flat_workgroup_size: 1024
    .name:           _Z12k_recon_mfmaPKDF16_PKDv8_DF16_PKfPf
    .private_segment_fixed_size: 0
    .sgpr_count:     25
    .sgpr_spill_count: 0
    .symbol:         _Z12k_recon_mfmaPKDF16_PKDv8_DF16_PKfPf.kd
    .uniform_work_group_size: 1
    .uses_dynamic_stack: false
    .vgpr_count:     84
    .vgpr_spill_count: 0
    .wavefront_size: 64
  - .agpr_count:     0
    .args:
      - .actual_access:  read_only
        .address_space:  global
        .offset:         0
        .size:           8
        .value_kind:     global_buffer
      - .actual_access:  read_only
        .address_space:  global
        .offset:         8
        .size:           8
        .value_kind:     global_buffer
      - .actual_access:  read_only
        .address_space:  global
        .offset:         16
        .size:           8
        .value_kind:     global_buffer
      - .actual_access:  write_only
        .address_space:  global
        .offset:         24
        .size:           8
        .value_kind:     global_buffer
      - .actual_access:  write_only
        .address_space:  global
        .offset:         32
        .size:           8
        .value_kind:     global_buffer
      - .actual_access:  write_only
        .address_space:  global
        .offset:         40
        .size:           8
        .value_kind:     global_buffer
      - .actual_access:  write_only
        .address_space:  global
        .offset:         48
        .size:           8
        .value_kind:     global_buffer
      - .actual_access:  write_only
        .address_space:  global
        .offset:         56
        .size:           8
        .value_kind:     global_buffer
      - .actual_access:  write_only
        .address_space:  global
        .offset:         64
        .size:           8
        .value_kind:     global_buffer
    .group_segment_fixed_size: 67600
    .kernarg_segment_align: 8
    .kernarg_segment_size: 72
    .language:       OpenCL C
    .language_version:
      - 2
      - 0
    .max_flat_workgroup_size: 512
    .name:           _Z11k_proj_mfmaPKDF16_PKDv8_DF16_PKfPfPS1_S6_PhS6_PDF16_
    .private_segment_fixed_size: 0
    .sgpr_count:     36
    .sgpr_spill_count: 0
    .symbol:         _Z11k_proj_mfmaPKDF16_PKDv8_DF16_PKfPfPS1_S6_PhS6_PDF16_.kd
    .uniform_work_group_size: 1
    .uses_dynamic_stack: false
    .vgpr_count:     155
    .vgpr_spill_count: 0
    .wavefront_size: 64
  - .agpr_count:     0
    .args:
      - .actual_access:  read_only
        .address_space:  global
        .offset:         0
        .size:           8
        .value_kind:     global_buffer
      - .actual_access:  read_only
        .address_space:  global
        .offset:         8
        .size:           8
        .value_kind:     global_buffer
      - .actual_access:  read_only
        .address_space:  global
        .offset:         16
        .size:           8
        .value_kind:     global_buffer
      - .actual_access:  read_only
        .address_space:  global
        .offset:         24
        .size:           8
        .value_kind:     global_buffer
      - .actual_access:  read_only
        .address_space:  global
        .offset:         32
        .size:           8
        .value_kind:     global_buffer
      - .actual_access:  read_only
        .address_space:  global
        .offset:         40
        .size:           8
        .value_kind:     global_buffer
      - .actual_access:  write_only
        .address_space:  global
        .offset:         48
        .size:           8
        .value_kind:     global_buffer
      - .actual_access:  write_only
        .address_space:  global
        .offset:         56
        .size:           8
        .value_kind:     global_buffer
      - .actual_access:  read_only
        .address_space:  global
        .offset:         64
        .size:           8
        .value_kind:     global_buffer
      - .actual_access:  read_only
        .address_space:  global
        .offset:         72
        .size:           8
        .value_kind:     global_buffer
      - .actual_access:  write_only
        .address_space:  global
        .offset:         80
        .size:           8
        .value_kind:     global_buffer
      - .actual_access:  write_only
        .address_space:  global
        .offset:         88
        .size:           8
        .value_kind:     global_buffer
    .group_segment_fixed_size: 65536
    .kernarg_segment_align: 8
    .kernarg_segment_size: 96
    .language:       OpenCL C
    .language_version:
      - 2
      - 0
    .max_flat_workgroup_size: 512
    .name:           _Z6k_attnPKDv8_DF16_PKfPKhS3_S3_S3_PfS6_S3_S3_PS_S7_
    .private_segment_fixed_size: 0
    .sgpr_count:     34
    .sgpr_spill_count: 0
    .symbol:         _Z6k_attnPKDv8_DF16_PKfPKhS3_S3_S3_PfS6_S3_S3_PS_S7_.kd
    .uniform_work_group_size: 1
    .uses_dynamic_stack: false
    .vgpr_count:     128
    .vgpr_spill_count: 0
    .wavefront_size: 64
  - .agpr_count:     8
    .args:
      - .actual_access:  read_only
        .address_space:  global
        .offset:         0
        .size:           8
        .value_kind:     global_buffer
      - .actual_access:  read_only
        .address_space:  global
        .offset:         8
        .size:           8
        .value_kind:     global_buffer
      - .actual_access:  read_only
        .address_space:  global
        .offset:         16
        .size:           8
        .value_kind:     global_buffer
      - .actual_access:  read_only
        .address_space:  global
        .offset:         24
        .size:           8
        .value_kind:     global_buffer
      - .actual_access:  read_only
        .address_space:  global
        .offset:         32
        .size:           8
        .value_kind:     global_buffer
      - .actual_access:  write_only
        .address_space:  global
        .offset:         40
        .size:           8
        .value_kind:     global_buffer
    .group_segment_fixed_size: 10560
    .kernarg_segment_align: 8
    .kernarg_segment_size: 48
    .language:       OpenCL C
    .language_version:
      - 2
      - 0
    .max_flat_workgroup_size: 256
    .name:           _Z8k_resid2PKDF16_PKfS0_S2_S2_PDF16_
    .private_segment_fixed_size: 0
    .sgpr_count:     38
    .sgpr_spill_count: 0
    .symbol:         _Z8k_resid2PKDF16_PKfS0_S2_S2_PDF16_.kd
    .uniform_work_group_size: 1
    .uses_dynamic_stack: false
    .vgpr_count:     120
    .vgpr_spill_count: 0
    .wavefront_size: 64
  - .agpr_count:     0
    .args:
      - .actual_access:  read_only
        .address_space:  global
        .offset:         0
        .size:           8
        .value_kind:     global_buffer
      - .actual_access:  read_only
        .address_space:  global
        .offset:         8
        .size:           8
        .value_kind:     global_buffer
      - .actual_access:  read_only
        .address_space:  global
        .offset:         16
        .size:           8
        .value_kind:     global_buffer
      - .actual_access:  read_only
        .address_space:  global
        .offset:         24
        .size:           8
        .value_kind:     global_buffer
      - .actual_access:  read_only
        .address_space:  global
        .offset:         32
        .size:           8
        .value_kind:     global_buffer
      - .actual_access:  read_only
        .address_space:  global
        .offset:         40
        .size:           8
        .value_kind:     global_buffer
      - .actual_access:  read_only
        .address_space:  global
        .offset:         48
        .size:           8
        .value_kind:     global_buffer
      - .actual_access:  read_only
        .address_space:  global
        .offset:         56
        .size:           8
        .value_kind:     global_buffer
      - .actual_access:  read_only
        .address_space:  global
        .offset:         64
        .size:           8
        .value_kind:     global_buffer
      - .actual_access:  read_only
        .address_space:  global
        .offset:         72
        .size:           8
        .value_kind:     global_buffer
      - .actual_access:  write_only
        .address_space:  global
        .offset:         80
        .size:           8
        .value_kind:     global_buffer
      - .actual_access:  read_only
        .address_space:  global
        .offset:         88
        .size:           8
        .value_kind:     global_buffer
      - .actual_access:  read_only
        .address_space:  global
        .offset:         96
        .size:           8
        .value_kind:     global_buffer
      - .actual_access:  read_only
        .address_space:  global
        .offset:         104
        .size:           8
        .value_kind:     global_buffer
      - .actual_access:  read_only
        .address_space:  global
        .offset:         112
        .size:           8
        .value_kind:     global_buffer
      - .actual_access:  read_only
        .address_space:  global
        .offset:         120
        .size:           8
        .value_kind:     global_buffer
      - .actual_access:  read_only
        .address_space:  global
        .offset:         128
        .size:           8
        .value_kind:     global_buffer
      - .actual_access:  write_only
        .address_space:  global
        .offset:         136
        .size:           8
        .value_kind:     global_buffer
    .group_segment_fixed_size: 21248
    .kernarg_segment_align: 8
    .kernarg_segment_size: 144
    .language:       OpenCL C
    .language_version:
      - 2
      - 0
    .max_flat_workgroup_size: 512
    .name:           _Z8k_embed2PKfS0_S0_S0_S0_S0_S0_S0_S0_S0_PDF16_S0_S0_S0_S0_S0_S0_PDv8_DF16_
    .private_segment_fixed_size: 0
    .sgpr_count:     78
    .sgpr_spill_count: 0
    .symbol:         _Z8k_embed2PKfS0_S0_S0_S0_S0_S0_S0_S0_S0_PDF16_S0_S0_S0_S0_S0_S0_PDv8_DF16_.kd
    .uniform_work_group_size: 1
    .uses_dynamic_stack: false
    .vgpr_count:     99
    .vgpr_spill_count: 0
    .wavefront_size: 64
